# prep phase w_in_f copy: the 4 row loads of an iteration issued together (one wait) instead of three serialized load/wait pairs
# speedup vs baseline: 1.0097x; 1.0001x over previous
; __device__ void phase_prep(KParams& p, int bid, int nb, char* smem) {
;     ...
;   for (size_t i0 = (size_t)bid * NTHREADS + tid; i0 < (size_t)D * 1024 / 4; i0 += (size_t)4 * nb * NTHREADS) {
;     float4 v[4];
; #pragma unroll
;     for (int u = 0; u < 4; ++u) {
;       const size_t i = i0 + (size_t)u * nb * NTHREADS;
;       const int k = (int)(i / 256), c4 = (int)(i % 256) * 4;
;       v[u] = (i < (size_t)D * 1024 / 4) ? *reinterpret_cast<const float4*>(p.w_in + (size_t)k * DIN + c4) : float4{0.f, 0.f, 0.f, 0.f};
;     }
; #pragma unroll
;     for (int u = 0; u < 4; ++u) {
;       const size_t i = i0 + (size_t)u * nb * NTHREADS;
;       const int k = (int)(i / 256), c4 = (int)(i % 256) * 4;
;       uint2 o; o.x = pack2(v[u].x, v[u].y); o.y = pack2(v[u].z, v[u].w);
;       if (i < (size_t)D * 1024 / 4) *reinterpret_cast<uint2*>(p.w_in_f + (size_t)k * 1024 + c4) = o;
;     }
;   }
.LBB0_36:
	v_and_b32_e32 v1, 0x3fc, v8
	v_lshlrev_b32_e32 v10, 2, v1
	s_waitcnt lgkmcnt(0)
	v_lshl_add_u64 v[22:23], s[18:19], 0, v[10:11]
	v_alignbit_b32 v2, v21, v20, 8
	v_mad_u64_u32 v[2:3], s[6:7], v2, s25, v[22:23]
	v_lshrrev_b32_e32 v4, 8, v21
	v_mad_u32_u24 v3, v4, s25, v3
	global_load_dwordx4 v[2:5], v[2:3], off
	v_lshl_add_u64 v[12:13], v[20:21], 0, s[16:17]
	v_cmp_gt_u64_e32 vcc, s[10:11], v[12:13]
	v_mov_b32_e32 v16, 0
	v_mov_b32_e32 v17, 0
	s_and_saveexec_b64 s[6:7], vcc
	s_cbranch_execz .LBB0_38
	v_alignbit_b32 v10, v13, v12, 8
	v_mad_u64_u32 v[14:15], s[8:9], v10, s25, v[22:23]
	v_lshrrev_b32_e32 v10, 8, v13
	v_mad_u32_u24 v15, v10, s25, v15
	global_load_dwordx4 v[100:103], v[14:15], off
.LBB0_38:
	s_or_b64 exec, exec, s[6:7]
	v_lshl_add_u64 v[24:25], s[22:23], 0, v[20:21]
	v_cmp_gt_u64_e64 s[6:7], s[10:11], v[24:25]
	v_mov_b32_e32 v14, 0
	v_mov_b32_e32 v18, 0
	v_mov_b32_e32 v19, 0
	s_and_saveexec_b64 s[8:9], s[6:7]
	s_cbranch_execz .LBB0_40
	v_alignbit_b32 v10, v25, v24, 8
	v_mad_u64_u32 v[18:19], s[40:41], v10, s25, v[22:23]
	v_lshrrev_b32_e32 v10, 8, v25
	v_mad_u32_u24 v19, v10, s25, v19
	global_load_dwordx4 v[104:107], v[18:19], off
.LBB0_40:
	s_or_b64 exec, exec, s[8:9]
	v_lshl_add_u64 v[20:21], s[28:29], 0, v[20:21]
	v_cmp_gt_u64_e64 s[8:9], s[10:11], v[20:21]
	v_mov_b32_e32 v15, 0
	s_and_saveexec_b64 s[40:41], s[8:9]
	s_cbranch_execz .LBB0_42
	v_alignbit_b32 v10, v21, v20, 8
	v_mad_u64_u32 v[14:15], s[42:43], v10, s25, v[22:23]
	v_lshrrev_b32_e32 v10, 8, v21
	v_mad_u32_u24 v15, v10, s25, v15
	global_load_dwordx4 v[108:111], v[14:15], off
.LBB0_42:
	s_or_b64 exec, exec, s[40:41]
	v_lshlrev_b32_e32 v10, 1, v1
	v_and_b32_e32 v1, 0x1ffc00, v8
	v_lshl_add_u64 v[20:21], s[20:21], 0, v[10:11]
	v_lshlrev_b32_e32 v10, 1, v1
	s_waitcnt vmcnt(0)
	s_mov_b64 s[40:41], exec
	s_and_b64 exec, s[40:41], vcc
	v_cvt_pk_bf16_f32 v17, v102, v103
	v_cvt_pk_bf16_f32 v16, v100, v101
	s_and_b64 exec, s[40:41], s[6:7]
	v_cvt_pk_bf16_f32 v19, v106, v107
	v_cvt_pk_bf16_f32 v18, v104, v105
	s_and_b64 exec, s[40:41], s[8:9]
	v_cvt_pk_bf16_f32 v15, v110, v111
	v_cvt_pk_bf16_f32 v14, v108, v109
	s_mov_b64 exec, s[40:41]
	v_cvt_pk_bf16_f32 v5, v4, v5
	v_cvt_pk_bf16_f32 v4, v2, v3
	v_lshl_add_u64 v[2:3], v[20:21], 0, v[10:11]
	global_store_dwordx2 v[2:3], v[4:5], off
	s_and_saveexec_b64 s[40:41], vcc
	s_cbranch_execnz .LBB0_45
	s_or_b64 exec, exec, s[40:41]
	s_and_saveexec_b64 s[40:41], s[6:7]
	s_cbranch_execnz .LBB0_46
